# attention unit epilogue: 16 head-gain loads hoisted out of the store loop (were 16 serialized store+load round trips)
# speedup vs baseline: 1.0038x; 1.0015x over previous
; #define GAS __attribute__((address_space(1)))
; #define WG_BAR() do { asm volatile("s_waitcnt vmcnt(0) lgkmcnt(0)" ::: "memory"); __builtin_amdgcn_s_barrier(); asm volatile("" ::: "memory"); } while (0)
; __device__ __forceinline__ unsigned pk2(float lo, float hi) { f32x2_t_ v = {lo, hi}; bf16x2_t_ b = __builtin_convertvector(v, bf16x2_t_); return __builtin_bit_cast(unsigned, b); }
; __device__ __forceinline__ float half_swap_sum(float m) { unsigned a = __builtin_bit_cast(unsigned, m), b = a; half_swap(a, b); return __builtin_bit_cast(float, a) + __builtin_bit_cast(float, b); }
; __device__ __forceinline__ void attn_unit(LAS unsigned char* lds, const bf16* proj, bf16* Y, const float* relb, const float* hgain, float lam, float oscale, int b, int h, int qb, int tid, int lane, int wid, Stopwatch& sw) {
;     ...
;     WG_BAR();
;     if (mp == 0) {
;         float ss = 0.f;
; #pragma unroll
;         for (int c = 0; c < 4; ++c)
; #pragma unroll
;             for (int r = 0; r < 16; ++r) { const float d = o[c][r] * inv - lam * xch[((wq * 64 + c * 16 + r) << 6) + lane]; o[c][r] = d; ss += d * d; }
;         ss = half_swap_sum(ss);
;         const float rs = oscale / sqrtf(ss * (1.f / 128.f) + NORM_EPS);
;         bf16* yp = Y + (rowbase + qi) * LDY + 1024 + h * 128;
; #pragma unroll
;         for (int c = 0; c < 4; ++c)
; #pragma unroll
;             for (int r4 = 0; r4 < 4; ++r4) { const int dv = 32 * c + 8 * r4 + 4 * hi; const f32x4 g = *(const GAS f32x4*)(hgain + dv);
;                 v2u w; w.x = pk2(o[c][4 * r4] * rs * g.x, o[c][4 * r4 + 1] * rs * g.y); w.y = pk2(o[c][4 * r4 + 2] * rs * g.z, o[c][4 * r4 + 3] * rs * g.w);
;                 *(GAS v2u*)(yp + dv) = w; }
.LBB0_444:
	s_waitcnt vmcnt(0) lgkmcnt(0)
	s_barrier
	s_andn2_b64 vcc, exec, s[72:73]
	s_cbranch_vccnz .LBB0_343
	global_load_dwordx4 v[136:139], v2, s[74:75]
	global_load_dwordx4 v[140:143], v2, s[74:75] offset:32
	global_load_dwordx4 v[144:147], v2, s[74:75] offset:64
	global_load_dwordx4 v[152:155], v2, s[74:75] offset:96
	global_load_dwordx4 v[156:159], v2, s[74:75] offset:128
	global_load_dwordx4 v[168:171], v2, s[74:75] offset:160
	global_load_dwordx4 v[172:175], v2, s[74:75] offset:192
	global_load_dwordx4 v[176:179], v2, s[74:75] offset:224
	global_load_dwordx4 v[180:183], v2, s[74:75] offset:256
	global_load_dwordx4 v[184:187], v2, s[74:75] offset:288
	global_load_dwordx4 v[188:191], v2, s[74:75] offset:320
	global_load_dwordx4 v[192:195], v2, s[74:75] offset:352
	global_load_dwordx4 v[204:207], v2, s[74:75] offset:384
	global_load_dwordx4 v[208:211], v2, s[74:75] offset:416
	global_load_dwordx4 v[212:215], v2, s[74:75] offset:448
	global_load_dwordx4 v[216:219], v2, s[74:75] offset:480
	v_readlane_b32 s0, v253, 9
	v_readlane_b32 s24, v253, 61
	v_readlane_b32 s25, v253, 62
	v_lshl_add_u32 v76, v166, 2, s0
	ds_read2st64_b32 v[70:71], v76 offset1:1
	ds_read2st64_b32 v[68:69], v76 offset0:2 offset1:3
	ds_read2st64_b32 v[74:75], v76 offset0:4 offset1:5
	ds_read2st64_b32 v[72:73], v76 offset0:6 offset1:7
	ds_read2st64_b32 v[78:79], v76 offset0:8 offset1:9
	ds_read2st64_b32 v[82:83], v76 offset0:10 offset1:11
	s_waitcnt lgkmcnt(7)
	ds_read2st64_b32 v[126:127], v76 offset0:12 offset1:13
	s_waitcnt lgkmcnt(7)
	ds_read2st64_b32 v[128:129], v76 offset0:14 offset1:15
	ds_read2st64_b32 v[130:131], v76 offset0:16 offset1:17
	ds_read2st64_b32 v[132:133], v76 offset0:18 offset1:19
	ds_read2st64_b32 v[122:123], v76 offset0:20 offset1:21
	ds_read2st64_b32 v[124:125], v76 offset0:22 offset1:23
	ds_read2st64_b32 v[118:119], v76 offset0:24 offset1:25
	ds_read2st64_b32 v[120:121], v76 offset0:26 offset1:27
	ds_read2st64_b32 v[114:115], v76 offset0:28 offset1:29
	ds_read2st64_b32 v[116:117], v76 offset0:30 offset1:31
	ds_read2st64_b32 v[110:111], v76 offset0:32 offset1:33
	ds_read2st64_b32 v[112:113], v76 offset0:34 offset1:35
	ds_read2st64_b32 v[106:107], v76 offset0:36 offset1:37
	ds_read2st64_b32 v[108:109], v76 offset0:38 offset1:39
	ds_read2st64_b32 v[102:103], v76 offset0:40 offset1:41
	ds_read2st64_b32 v[104:105], v76 offset0:42 offset1:43
	ds_read2st64_b32 v[98:99], v76 offset0:44 offset1:45
	ds_read2st64_b32 v[100:101], v76 offset0:46 offset1:47
	ds_read2st64_b32 v[94:95], v76 offset0:48 offset1:49
	ds_read2st64_b32 v[96:97], v76 offset0:50 offset1:51
	ds_read2st64_b32 v[90:91], v76 offset0:52 offset1:53
	ds_read2st64_b32 v[92:93], v76 offset0:54 offset1:55
	ds_read2st64_b32 v[86:87], v76 offset0:56 offset1:57
	ds_read2st64_b32 v[88:89], v76 offset0:58 offset1:59
	ds_read2st64_b32 v[84:85], v76 offset0:60 offset1:61
	ds_read2st64_b32 v[76:77], v76 offset0:62 offset1:63
	s_waitcnt lgkmcnt(14)
	v_pk_mul_f32 v[68:69], v[148:149], v[68:69]
	s_lshl_b32 s34, s18, 1
	v_pk_fma_f32 v[68:69], v[54:55], v[80:81], v[68:69] op_sel_hi:[1,0,1] neg_lo:[0,0,1] neg_hi:[0,0,1]
	v_pk_mul_f32 v[54:55], v[148:149], v[70:71]
	s_waitcnt lgkmcnt(0)
	v_pk_mul_f32 v[76:77], v[148:149], v[76:77]
	v_pk_fma_f32 v[70:71], v[52:53], v[80:81], v[54:55] op_sel_hi:[1,0,1] neg_lo:[0,0,1] neg_hi:[0,0,1]
	v_pk_fma_f32 v[18:19], v[18:19], v[80:81], v[76:77] op_sel_hi:[1,0,1] neg_lo:[0,0,1] neg_hi:[0,0,1]
	v_mov_b64_e32 v[76:77], s[24:25]
	v_mad_u64_u32 v[76:77], s[24:25], v151, s67, v[76:77]
	v_mov_b32_e32 v134, v77
	v_mad_u64_u32 v[134:135], s[24:25], v163, s67, v[134:135]
	v_mul_f32_e32 v52, v71, v71
	v_mov_b32_e32 v77, v134
	v_pk_fma_f32 v[52:53], v[70:71], v[70:71], v[52:53] op_sel_hi:[1,1,0]
	v_pk_mul_f32 v[72:73], v[148:149], v[72:73]
	v_lshl_add_u64 v[76:77], v[76:77], 0, s[34:35]
	v_pk_fma_f32 v[52:53], v[68:69], v[68:69], v[52:53]
	v_mul_f32_e32 v54, v69, v69
	v_mov_b32_e32 v151, v3
	v_pk_fma_f32 v[72:73], v[58:59], v[80:81], v[72:73] op_sel_hi:[1,0,1] neg_lo:[0,0,1] neg_hi:[0,0,1]
	v_pk_mul_f32 v[58:59], v[148:149], v[74:75]
	v_pk_add_f32 v[54:55], v[52:53], v[54:55] op_sel_hi:[1,0]
	v_lshl_add_u64 v[52:53], v[76:77], 0, v[150:151]
	v_pk_fma_f32 v[76:77], v[56:57], v[80:81], v[58:59] op_sel_hi:[1,0,1] neg_lo:[0,0,1] neg_hi:[0,0,1]
	s_nop 0
	v_pk_fma_f32 v[54:55], v[76:77], v[76:77], v[54:55]
	v_mul_f32_e32 v56, v77, v77
	v_pk_add_f32 v[54:55], v[54:55], v[56:57] op_sel_hi:[1,0]
	v_mul_f32_e32 v56, v73, v73
	v_pk_fma_f32 v[54:55], v[72:73], v[72:73], v[54:55]
	s_nop 0
	v_pk_add_f32 v[54:55], v[54:55], v[56:57] op_sel_hi:[1,0]
	v_pk_mul_f32 v[56:57], v[148:149], v[82:83]
	s_nop 0
	v_pk_fma_f32 v[74:75], v[62:63], v[80:81], v[56:57] op_sel_hi:[1,0,1] neg_lo:[0,0,1] neg_hi:[0,0,1]
	v_pk_mul_f32 v[56:57], v[148:149], v[78:79]
	s_nop 0
	v_pk_fma_f32 v[82:83], v[60:61], v[80:81], v[56:57] op_sel_hi:[1,0,1] neg_lo:[0,0,1] neg_hi:[0,0,1]
	s_nop 0
	v_pk_fma_f32 v[54:55], v[82:83], v[82:83], v[54:55]
	v_mul_f32_e32 v56, v83, v83
	v_pk_add_f32 v[54:55], v[54:55], v[56:57] op_sel_hi:[1,0]
	v_mul_f32_e32 v56, v75, v75
	v_pk_fma_f32 v[54:55], v[74:75], v[74:75], v[54:55]
	s_nop 0
	v_pk_add_f32 v[54:55], v[54:55], v[56:57] op_sel_hi:[1,0]
	v_pk_mul_f32 v[56:57], v[148:149], v[128:129]
	s_nop 0
	v_pk_fma_f32 v[66:67], v[66:67], v[80:81], v[56:57] op_sel_hi:[1,0,1] neg_lo:[0,0,1] neg_hi:[0,0,1]
	v_pk_mul_f32 v[56:57], v[148:149], v[126:127]
	s_nop 0
	v_pk_fma_f32 v[78:79], v[64:65], v[80:81], v[56:57] op_sel_hi:[1,0,1] neg_lo:[0,0,1] neg_hi:[0,0,1]
	s_nop 0
	v_pk_fma_f32 v[54:55], v[78:79], v[78:79], v[54:55]
	v_mul_f32_e32 v56, v79, v79
	v_pk_add_f32 v[54:55], v[54:55], v[56:57] op_sel_hi:[1,0]
; __device__ __forceinline__ float half_swap_sum(float m) { unsigned a = __builtin_bit_cast(unsigned, m), b = a; half_swap(a, b); return __builtin_bit_cast(float, a) + __builtin_bit_cast(float, b); }
; __device__ __forceinline__ void attn_unit(LAS unsigned char* lds, const bf16* proj, bf16* Y, const float* relb, const float* hgain, float lam, float oscale, int b, int h, int qb, int tid, int lane, int wid, Stopwatch& sw) {
;     ...
;     if (mp == 0) {
;         float ss = 0.f;
; #pragma unroll
;         for (int c = 0; c < 4; ++c)
; #pragma unroll
;             for (int r = 0; r < 16; ++r) { const float d = o[c][r] * inv - lam * xch[((wq * 64 + c * 16 + r) << 6) + lane]; o[c][r] = d; ss += d * d; }
;         ss = half_swap_sum(ss);
	v_mul_f32_e32 v56, v67, v67
	v_pk_fma_f32 v[54:55], v[66:67], v[66:67], v[54:55]
	s_nop 0
	v_pk_add_f32 v[54:55], v[54:55], v[56:57] op_sel_hi:[1,0]
	v_pk_mul_f32 v[56:57], v[148:149], v[132:133]
	s_nop 0
	v_pk_fma_f32 v[60:61], v[38:39], v[80:81], v[56:57] op_sel_hi:[1,0,1] neg_lo:[0,0,1] neg_hi:[0,0,1]
	v_pk_mul_f32 v[38:39], v[148:149], v[130:131]
	s_nop 0
	v_pk_fma_f32 v[64:65], v[36:37], v[80:81], v[38:39] op_sel_hi:[1,0,1] neg_lo:[0,0,1] neg_hi:[0,0,1]
	s_nop 0
	v_pk_fma_f32 v[36:37], v[64:65], v[64:65], v[54:55]
	v_mul_f32_e32 v38, v65, v65
	v_pk_add_f32 v[36:37], v[36:37], v[38:39] op_sel_hi:[1,0]
	v_mul_f32_e32 v38, v61, v61
	v_pk_fma_f32 v[36:37], v[60:61], v[60:61], v[36:37]
	s_nop 0
	v_pk_add_f32 v[36:37], v[36:37], v[38:39] op_sel_hi:[1,0]
	v_pk_mul_f32 v[38:39], v[148:149], v[124:125]
	s_nop 0
	v_pk_fma_f32 v[56:57], v[42:43], v[80:81], v[38:39] op_sel_hi:[1,0,1] neg_lo:[0,0,1] neg_hi:[0,0,1]
	v_pk_mul_f32 v[38:39], v[148:149], v[122:123]
	s_nop 0
	v_pk_fma_f32 v[62:63], v[40:41], v[80:81], v[38:39] op_sel_hi:[1,0,1] neg_lo:[0,0,1] neg_hi:[0,0,1]
	s_nop 0
	v_pk_fma_f32 v[36:37], v[62:63], v[62:63], v[36:37]
	v_mul_f32_e32 v38, v63, v63
	v_pk_add_f32 v[36:37], v[36:37], v[38:39] op_sel_hi:[1,0]
	v_mul_f32_e32 v38, v57, v57
	v_pk_fma_f32 v[36:37], v[56:57], v[56:57], v[36:37]
	s_nop 0
	v_pk_add_f32 v[36:37], v[36:37], v[38:39] op_sel_hi:[1,0]
	v_pk_mul_f32 v[38:39], v[148:149], v[120:121]
	s_nop 0
	v_pk_fma_f32 v[54:55], v[46:47], v[80:81], v[38:39] op_sel_hi:[1,0,1] neg_lo:[0,0,1] neg_hi:[0,0,1]
	v_pk_mul_f32 v[38:39], v[148:149], v[118:119]
	s_nop 0
	v_pk_fma_f32 v[58:59], v[44:45], v[80:81], v[38:39] op_sel_hi:[1,0,1] neg_lo:[0,0,1] neg_hi:[0,0,1]
	s_nop 0
	v_pk_fma_f32 v[36:37], v[58:59], v[58:59], v[36:37]
	v_mul_f32_e32 v38, v59, v59
	v_pk_add_f32 v[36:37], v[36:37], v[38:39] op_sel_hi:[1,0]
	v_mul_f32_e32 v38, v55, v55
	v_pk_fma_f32 v[36:37], v[54:55], v[54:55], v[36:37]
	s_nop 0
	v_pk_add_f32 v[36:37], v[36:37], v[38:39] op_sel_hi:[1,0]
	v_pk_mul_f32 v[38:39], v[148:149], v[116:117]
	s_nop 0
	v_pk_fma_f32 v[44:45], v[50:51], v[80:81], v[38:39] op_sel_hi:[1,0,1] neg_lo:[0,0,1] neg_hi:[0,0,1]
	v_pk_mul_f32 v[38:39], v[148:149], v[114:115]
	s_nop 0
	v_pk_fma_f32 v[48:49], v[48:49], v[80:81], v[38:39] op_sel_hi:[1,0,1] neg_lo:[0,0,1] neg_hi:[0,0,1]
	s_nop 0
	v_pk_fma_f32 v[36:37], v[48:49], v[48:49], v[36:37]
	v_mul_f32_e32 v38, v49, v49
	v_pk_add_f32 v[36:37], v[36:37], v[38:39] op_sel_hi:[1,0]
	v_mul_f32_e32 v38, v45, v45
	v_pk_fma_f32 v[36:37], v[44:45], v[44:45], v[36:37]
	s_nop 0
	v_pk_add_f32 v[36:37], v[36:37], v[38:39] op_sel_hi:[1,0]
	v_pk_mul_f32 v[38:39], v[148:149], v[112:113]
	s_nop 0
	v_pk_fma_f32 v[40:41], v[22:23], v[80:81], v[38:39] op_sel_hi:[1,0,1] neg_lo:[0,0,1] neg_hi:[0,0,1]
	v_pk_mul_f32 v[22:23], v[148:149], v[110:111]
	s_nop 0
	v_pk_fma_f32 v[46:47], v[20:21], v[80:81], v[22:23] op_sel_hi:[1,0,1] neg_lo:[0,0,1] neg_hi:[0,0,1]
	s_nop 0
	v_pk_fma_f32 v[20:21], v[46:47], v[46:47], v[36:37]
	v_mul_f32_e32 v22, v47, v47
	v_pk_add_f32 v[20:21], v[20:21], v[22:23] op_sel_hi:[1,0]
	v_mul_f32_e32 v22, v41, v41
	v_pk_fma_f32 v[20:21], v[40:41], v[40:41], v[20:21]
	s_nop 0
	v_pk_add_f32 v[20:21], v[20:21], v[22:23] op_sel_hi:[1,0]
	v_pk_mul_f32 v[22:23], v[148:149], v[108:109]
	s_nop 0
	v_pk_fma_f32 v[36:37], v[26:27], v[80:81], v[22:23] op_sel_hi:[1,0,1] neg_lo:[0,0,1] neg_hi:[0,0,1]
	v_pk_mul_f32 v[22:23], v[148:149], v[106:107]
	s_nop 0
	v_pk_fma_f32 v[42:43], v[24:25], v[80:81], v[22:23] op_sel_hi:[1,0,1] neg_lo:[0,0,1] neg_hi:[0,0,1]
	s_nop 0
	v_pk_fma_f32 v[20:21], v[42:43], v[42:43], v[20:21]
	v_mul_f32_e32 v22, v43, v43
	v_pk_add_f32 v[20:21], v[20:21], v[22:23] op_sel_hi:[1,0]
	v_mul_f32_e32 v22, v37, v37
	v_pk_fma_f32 v[20:21], v[36:37], v[36:37], v[20:21]
	s_nop 0
	v_pk_add_f32 v[20:21], v[20:21], v[22:23] op_sel_hi:[1,0]
	v_pk_mul_f32 v[22:23], v[148:149], v[104:105]
	s_nop 0
	v_pk_fma_f32 v[30:31], v[30:31], v[80:81], v[22:23] op_sel_hi:[1,0,1] neg_lo:[0,0,1] neg_hi:[0,0,1]
	v_pk_mul_f32 v[22:23], v[148:149], v[102:103]
	s_nop 0
	v_pk_fma_f32 v[38:39], v[28:29], v[80:81], v[22:23] op_sel_hi:[1,0,1] neg_lo:[0,0,1] neg_hi:[0,0,1]
	s_nop 0
	v_pk_fma_f32 v[20:21], v[38:39], v[38:39], v[20:21]
	v_mul_f32_e32 v22, v39, v39
	v_pk_add_f32 v[20:21], v[20:21], v[22:23] op_sel_hi:[1,0]
	v_mul_f32_e32 v22, v31, v31
	v_pk_fma_f32 v[20:21], v[30:31], v[30:31], v[20:21]
	s_nop 0
	v_pk_add_f32 v[20:21], v[20:21], v[22:23] op_sel_hi:[1,0]
	v_pk_mul_f32 v[22:23], v[148:149], v[100:101]
	s_nop 0
	v_pk_fma_f32 v[24:25], v[34:35], v[80:81], v[22:23] op_sel_hi:[1,0,1] neg_lo:[0,0,1] neg_hi:[0,0,1]
	v_pk_mul_f32 v[22:23], v[148:149], v[98:99]
	s_nop 0
	v_pk_fma_f32 v[28:29], v[32:33], v[80:81], v[22:23] op_sel_hi:[1,0,1] neg_lo:[0,0,1] neg_hi:[0,0,1]
	s_nop 0
	v_pk_fma_f32 v[20:21], v[28:29], v[28:29], v[20:21]
	v_mul_f32_e32 v22, v29, v29
	v_pk_add_f32 v[20:21], v[20:21], v[22:23] op_sel_hi:[1,0]
	v_mul_f32_e32 v22, v25, v25
	v_pk_fma_f32 v[20:21], v[24:25], v[24:25], v[20:21]
	s_nop 0
	v_pk_add_f32 v[22:23], v[20:21], v[22:23] op_sel_hi:[1,0]
	v_pk_mul_f32 v[20:21], v[148:149], v[96:97]
	s_nop 0
	v_pk_fma_f32 v[20:21], v[6:7], v[80:81], v[20:21] op_sel_hi:[1,0,1] neg_lo:[0,0,1] neg_hi:[0,0,1]
	v_pk_mul_f32 v[6:7], v[148:149], v[94:95]
	s_nop 0
	v_pk_fma_f32 v[26:27], v[4:5], v[80:81], v[6:7] op_sel_hi:[1,0,1] neg_lo:[0,0,1] neg_hi:[0,0,1]
	s_nop 0
	v_pk_fma_f32 v[4:5], v[26:27], v[26:27], v[22:23]
	v_mul_f32_e32 v6, v27, v27
	v_pk_add_f32 v[4:5], v[4:5], v[6:7] op_sel_hi:[1,0]
	v_mul_f32_e32 v6, v21, v21
	v_pk_fma_f32 v[4:5], v[20:21], v[20:21], v[4:5]
	s_nop 0
	v_pk_add_f32 v[4:5], v[4:5], v[6:7] op_sel_hi:[1,0]
; #define GAS __attribute__((address_space(1)))
; __device__ __forceinline__ unsigned pk2(float lo, float hi) { f32x2_t_ v = {lo, hi}; bf16x2_t_ b = __builtin_convertvector(v, bf16x2_t_); return __builtin_bit_cast(unsigned, b); }
; __device__ __forceinline__ float half_swap_sum(float m) { unsigned a = __builtin_bit_cast(unsigned, m), b = a; half_swap(a, b); return __builtin_bit_cast(float, a) + __builtin_bit_cast(float, b); }
; __device__ __forceinline__ void attn_unit(LAS unsigned char* lds, const bf16* proj, bf16* Y, const float* relb, const float* hgain, float lam, float oscale, int b, int h, int qb, int tid, int lane, int wid, Stopwatch& sw) {
;     ...
;             for (int r = 0; r < 16; ++r) { const float d = o[c][r] * inv - lam * xch[((wq * 64 + c * 16 + r) << 6) + lane]; o[c][r] = d; ss += d * d; }
;         ss = half_swap_sum(ss);
;         const float rs = oscale / sqrtf(ss * (1.f / 128.f) + NORM_EPS);
;         bf16* yp = Y + (rowbase + qi) * LDY + 1024 + h * 128;
; #pragma unroll
;         for (int c = 0; c < 4; ++c)
; #pragma unroll
;             for (int r4 = 0; r4 < 4; ++r4) { const int dv = 32 * c + 8 * r4 + 4 * hi; const f32x4 g = *(const GAS f32x4*)(hgain + dv);
;                 v2u w; w.x = pk2(o[c][4 * r4] * rs * g.x, o[c][4 * r4 + 1] * rs * g.y); w.y = pk2(o[c][4 * r4 + 2] * rs * g.z, o[c][4 * r4 + 3] * rs * g.w);
;                 *(GAS v2u*)(yp + dv) = w; }
	v_pk_mul_f32 v[6:7], v[148:149], v[92:93]
	s_nop 0
	v_pk_fma_f32 v[10:11], v[10:11], v[80:81], v[6:7] op_sel_hi:[1,0,1] neg_lo:[0,0,1] neg_hi:[0,0,1]
	v_pk_mul_f32 v[6:7], v[148:149], v[90:91]
	s_nop 0
	v_pk_fma_f32 v[22:23], v[8:9], v[80:81], v[6:7] op_sel_hi:[1,0,1] neg_lo:[0,0,1] neg_hi:[0,0,1]
	v_pk_mul_f32 v[8:9], v[148:149], v[86:87]
	v_pk_fma_f32 v[4:5], v[22:23], v[22:23], v[4:5]
	v_mul_f32_e32 v6, v23, v23
	v_pk_add_f32 v[4:5], v[4:5], v[6:7] op_sel_hi:[1,0]
	v_mul_f32_e32 v6, v11, v11
	v_pk_fma_f32 v[4:5], v[10:11], v[10:11], v[4:5]
	v_pk_fma_f32 v[8:9], v[12:13], v[80:81], v[8:9] op_sel_hi:[1,0,1] neg_lo:[0,0,1] neg_hi:[0,0,1]
	v_pk_add_f32 v[6:7], v[4:5], v[6:7] op_sel_hi:[1,0]
	v_pk_mul_f32 v[4:5], v[148:149], v[88:89]
	v_pk_fma_f32 v[6:7], v[8:9], v[8:9], v[6:7]
	v_mul_f32_e32 v12, v9, v9
	v_pk_fma_f32 v[4:5], v[14:15], v[80:81], v[4:5] op_sel_hi:[1,0,1] neg_lo:[0,0,1] neg_hi:[0,0,1]
	v_pk_add_f32 v[6:7], v[6:7], v[12:13] op_sel_hi:[1,0]
	v_mul_f32_e32 v12, v5, v5
	v_pk_fma_f32 v[6:7], v[4:5], v[4:5], v[6:7]
	s_nop 0
	v_pk_add_f32 v[12:13], v[6:7], v[12:13] op_sel_hi:[1,0]
	v_pk_mul_f32 v[6:7], v[148:149], v[84:85]
	s_nop 0
	v_pk_fma_f32 v[6:7], v[16:17], v[80:81], v[6:7] op_sel_hi:[1,0,1] neg_lo:[0,0,1] neg_hi:[0,0,1]
	s_nop 0
	v_pk_fma_f32 v[12:13], v[6:7], v[6:7], v[12:13]
	v_mul_f32_e32 v14, v7, v7
	v_pk_add_f32 v[12:13], v[12:13], v[14:15] op_sel_hi:[1,0]
	v_mul_f32_e32 v14, v19, v19
	v_pk_fma_f32 v[12:13], v[18:19], v[18:19], v[12:13]
	s_nop 0
	v_pk_add_f32 v[12:13], v[12:13], v[14:15] op_sel_hi:[1,0]
	s_nop 0
	v_mov_b32_e32 v13, v12
	s_nop 1
	v_permlane32_swap_b32 v12, v13
	s_nop 1
	s_nop 0
	v_add_f32_e32 v12, v12, v13
	v_fmamk_f32 v12, v12, 0x3c000000, v240
	v_cmp_gt_f32_e32 vcc, s82, v12
	v_mul_f32_e32 v13, 0x4f800000, v12
	s_nop 0
	v_cndmask_b32_e32 v12, v12, v13, vcc
	v_sqrt_f32_e32 v13, v12
	s_nop 0
	v_add_u32_e32 v14, -1, v13
	v_fma_f32 v15, -v14, v13, v12
	v_cmp_ge_f32_e64 s[36:37], 0, v15
	v_add_u32_e32 v15, 1, v13
	s_nop 0
	v_cndmask_b32_e64 v14, v13, v14, s[36:37]
	v_fma_f32 v13, -v15, v13, v12
	v_cmp_lt_f32_e64 s[36:37], 0, v13
	s_nop 1
	v_cndmask_b32_e64 v13, v14, v15, s[36:37]
	v_mul_f32_e32 v14, 0x37800000, v13
	v_cndmask_b32_e32 v13, v13, v14, vcc
	v_cmp_class_f32_e32 vcc, v12, v241
	s_nop 1
	v_cndmask_b32_e32 v12, v13, v12, vcc
	v_div_scale_f32 v13, s[18:19], v12, v12, v162
	v_rcp_f32_e32 v14, v13
	s_nop 0
	v_fma_f32 v15, -v13, v14, 1.0
	v_fmac_f32_e32 v14, v15, v14
	v_div_scale_f32 v15, vcc, v162, v12, v162
	v_mul_f32_e32 v16, v15, v14
	v_fma_f32 v17, -v13, v16, v15
	v_fmac_f32_e32 v16, v17, v14
	v_fma_f32 v13, -v13, v16, v15
	v_div_fmas_f32 v13, v13, v14, v16
	v_div_fixup_f32 v12, v13, v12, v162
	v_pk_mul_f32 v[32:33], v[70:71], v[12:13] op_sel_hi:[1,0]
	v_pk_mul_f32 v[30:31], v[30:31], v[12:13] op_sel_hi:[1,0]
	v_pk_mul_f32 v[28:29], v[28:29], v[12:13] op_sel_hi:[1,0]
	v_pk_mul_f32 v[24:25], v[24:25], v[12:13] op_sel_hi:[1,0]
	v_pk_mul_f32 v[20:21], v[20:21], v[12:13] op_sel_hi:[1,0]
	v_pk_mul_f32 v[10:11], v[10:11], v[12:13] op_sel_hi:[1,0]
	v_pk_mul_f32 v[8:9], v[8:9], v[12:13] op_sel_hi:[1,0]
	v_pk_mul_f32 v[4:5], v[4:5], v[12:13] op_sel_hi:[1,0]
	s_waitcnt vmcnt(0)
; #define GAS __attribute__((address_space(1)))
; __device__ __forceinline__ unsigned pk2(float lo, float hi) { f32x2_t_ v = {lo, hi}; bf16x2_t_ b = __builtin_convertvector(v, bf16x2_t_); return __builtin_bit_cast(unsigned, b); }
; __device__ __forceinline__ void attn_unit(LAS unsigned char* lds, const bf16* proj, bf16* Y, const float* relb, const float* hgain, float lam, float oscale, int b, int h, int qb, int tid, int lane, int wid, Stopwatch& sw) {
;     ...
; #pragma unroll
;         for (int c = 0; c < 4; ++c)
; #pragma unroll
;             for (int r4 = 0; r4 < 4; ++r4) { const int dv = 32 * c + 8 * r4 + 4 * hi; const f32x4 g = *(const GAS f32x4*)(hgain + dv);
;                 v2u w; w.x = pk2(o[c][4 * r4] * rs * g.x, o[c][4 * r4 + 1] * rs * g.y); w.y = pk2(o[c][4 * r4 + 2] * rs * g.z, o[c][4 * r4 + 3] * rs * g.w);
;                 *(GAS v2u*)(yp + dv) = w; }
	v_pk_mul_f32 v[14:15], v[136:137], v[32:33]
	v_pk_mul_f32 v[32:33], v[68:69], v[12:13] op_sel_hi:[1,0]
	v_cvt_pk_bf16_f32 v14, v14, v15
	v_pk_mul_f32 v[16:17], v[138:139], v[32:33]
	v_pk_mul_f32 v[32:33], v[76:77], v[12:13] op_sel_hi:[1,0]
	v_cvt_pk_bf16_f32 v15, v16, v17
	global_store_dwordx2 v[52:53], v[14:15], off offset:2048
	v_pk_mul_f32 v[14:15], v[140:141], v[32:33]
	v_pk_mul_f32 v[32:33], v[72:73], v[12:13] op_sel_hi:[1,0]
	v_cvt_pk_bf16_f32 v14, v14, v15
	v_pk_mul_f32 v[16:17], v[142:143], v[32:33]
	v_pk_mul_f32 v[32:33], v[82:83], v[12:13] op_sel_hi:[1,0]
	v_cvt_pk_bf16_f32 v15, v16, v17
	global_store_dwordx2 v[52:53], v[14:15], off offset:2064
	v_pk_mul_f32 v[14:15], v[144:145], v[32:33]
	v_pk_mul_f32 v[32:33], v[74:75], v[12:13] op_sel_hi:[1,0]
	v_cvt_pk_bf16_f32 v14, v14, v15
	v_pk_mul_f32 v[16:17], v[146:147], v[32:33]
	v_pk_mul_f32 v[32:33], v[78:79], v[12:13] op_sel_hi:[1,0]
	v_cvt_pk_bf16_f32 v15, v16, v17
	global_store_dwordx2 v[52:53], v[14:15], off offset:2080
	v_pk_mul_f32 v[14:15], v[152:153], v[32:33]
	v_pk_mul_f32 v[32:33], v[66:67], v[12:13] op_sel_hi:[1,0]
	v_cvt_pk_bf16_f32 v14, v14, v15
	v_pk_mul_f32 v[16:17], v[154:155], v[32:33]
	v_pk_mul_f32 v[32:33], v[64:65], v[12:13] op_sel_hi:[1,0]
	v_cvt_pk_bf16_f32 v15, v16, v17
	global_store_dwordx2 v[52:53], v[14:15], off offset:2096
	v_pk_mul_f32 v[14:15], v[32:33], v[156:157]
	v_pk_mul_f32 v[32:33], v[60:61], v[12:13] op_sel_hi:[1,0]
	v_cvt_pk_bf16_f32 v14, v14, v15
	v_pk_mul_f32 v[16:17], v[32:33], v[158:159]
	v_pk_mul_f32 v[32:33], v[62:63], v[12:13] op_sel_hi:[1,0]
	v_cvt_pk_bf16_f32 v15, v16, v17
	global_store_dwordx2 v[52:53], v[14:15], off offset:2112
	v_pk_mul_f32 v[14:15], v[32:33], v[168:169]
	v_pk_mul_f32 v[32:33], v[56:57], v[12:13] op_sel_hi:[1,0]
	v_cvt_pk_bf16_f32 v14, v14, v15
	v_pk_mul_f32 v[16:17], v[32:33], v[170:171]
	v_pk_mul_f32 v[32:33], v[58:59], v[12:13] op_sel_hi:[1,0]
	v_cvt_pk_bf16_f32 v15, v16, v17
	global_store_dwordx2 v[52:53], v[14:15], off offset:2128
	v_pk_mul_f32 v[14:15], v[32:33], v[172:173]
	v_pk_mul_f32 v[32:33], v[54:55], v[12:13] op_sel_hi:[1,0]
	v_cvt_pk_bf16_f32 v14, v14, v15
	v_pk_mul_f32 v[16:17], v[32:33], v[174:175]
	v_pk_mul_f32 v[32:33], v[48:49], v[12:13] op_sel_hi:[1,0]
	v_cvt_pk_bf16_f32 v15, v16, v17
	global_store_dwordx2 v[52:53], v[14:15], off offset:2144
	v_pk_mul_f32 v[14:15], v[32:33], v[176:177]
	v_pk_mul_f32 v[32:33], v[44:45], v[12:13] op_sel_hi:[1,0]
	v_cvt_pk_bf16_f32 v14, v14, v15
	v_pk_mul_f32 v[16:17], v[32:33], v[178:179]
	v_pk_mul_f32 v[32:33], v[46:47], v[12:13] op_sel_hi:[1,0]
	v_cvt_pk_bf16_f32 v15, v16, v17
	global_store_dwordx2 v[52:53], v[14:15], off offset:2160
	v_pk_mul_f32 v[14:15], v[32:33], v[180:181]
	v_pk_mul_f32 v[32:33], v[40:41], v[12:13] op_sel_hi:[1,0]
	v_cvt_pk_bf16_f32 v14, v14, v15
	v_pk_mul_f32 v[16:17], v[32:33], v[182:183]
	v_pk_mul_f32 v[32:33], v[42:43], v[12:13] op_sel_hi:[1,0]
	v_cvt_pk_bf16_f32 v15, v16, v17
	global_store_dwordx2 v[52:53], v[14:15], off offset:2176
	v_pk_mul_f32 v[14:15], v[32:33], v[184:185]
	v_pk_mul_f32 v[32:33], v[36:37], v[12:13] op_sel_hi:[1,0]
	v_cvt_pk_bf16_f32 v14, v14, v15
	v_pk_mul_f32 v[16:17], v[32:33], v[186:187]
	v_pk_mul_f32 v[32:33], v[38:39], v[12:13] op_sel_hi:[1,0]
	v_cvt_pk_bf16_f32 v15, v16, v17
	global_store_dwordx2 v[52:53], v[14:15], off offset:2192
	v_pk_mul_f32 v[14:15], v[32:33], v[188:189]
	v_pk_mul_f32 v[16:17], v[30:31], v[190:191]
	v_cvt_pk_bf16_f32 v14, v14, v15
	v_cvt_pk_bf16_f32 v15, v16, v17
	global_store_dwordx2 v[52:53], v[14:15], off offset:2208
	v_pk_mul_f32 v[14:15], v[28:29], v[192:193]
	v_pk_mul_f32 v[16:17], v[24:25], v[194:195]
	v_cvt_pk_bf16_f32 v14, v14, v15
	v_cvt_pk_bf16_f32 v15, v16, v17
	global_store_dwordx2 v[52:53], v[14:15], off offset:2224
	v_pk_mul_f32 v[24:25], v[26:27], v[12:13] op_sel_hi:[1,0]
	v_pk_mul_f32 v[16:17], v[20:21], v[206:207]
	v_pk_mul_f32 v[14:15], v[24:25], v[204:205]
	v_pk_mul_f32 v[20:21], v[22:23], v[12:13] op_sel_hi:[1,0]
	v_cvt_pk_bf16_f32 v14, v14, v15
	v_cvt_pk_bf16_f32 v15, v16, v17
	global_store_dwordx2 v[52:53], v[14:15], off offset:2240
	v_pk_mul_f32 v[14:15], v[20:21], v[208:209]
	v_pk_mul_f32 v[10:11], v[10:11], v[210:211]
	v_cvt_pk_bf16_f32 v14, v14, v15
	v_cvt_pk_bf16_f32 v15, v10, v11
	global_store_dwordx2 v[52:53], v[14:15], off offset:2256
	v_pk_mul_f32 v[8:9], v[8:9], v[212:213]
	v_pk_mul_f32 v[4:5], v[4:5], v[214:215]
	v_cvt_pk_bf16_f32 v8, v8, v9
	v_cvt_pk_bf16_f32 v9, v4, v5
	global_store_dwordx2 v[52:53], v[8:9], off offset:2272
	v_pk_mul_f32 v[4:5], v[6:7], v[12:13] op_sel_hi:[1,0]
	v_pk_mul_f32 v[6:7], v[18:19], v[12:13] op_sel_hi:[1,0]
	v_pk_mul_f32 v[4:5], v[4:5], v[216:217]
	v_pk_mul_f32 v[6:7], v[6:7], v[218:219]
	v_cvt_pk_bf16_f32 v4, v4, v5
	v_cvt_pk_bf16_f32 v5, v6, v7
	global_store_dwordx2 v[52:53], v[4:5], off offset:2288
	s_branch .LBB0_343
